# speedup vs baseline: 1.0144x; 1.0144x over previous
.Lstag_done_p1:
	s_lshr_b32 s22, s2, 3
	s_sub_i32 s22, 0xbf, s22
	s_and_b32 s2, s2, 7
	s_lshl_b32 s22, s22, 3
	s_or_b32 s2, s2, s22
	s_ashr_i32 s15, s2, 3
	s_mul_hi_i32 s14, s15, 0x55555556
	s_lshr_b32 s12, s14, 31
	s_add_i32 s14, s14, s12
	s_mul_i32 s16, s14, 0x3fffffd
	s_add_i32 s16, s16, s15
	s_lshl_b32 s15, s16, 6
	s_lshl_b32 s16, s2, 5
	s_and_b32 s16, s16, 32
	s_or_b32 s15, s15, s16
	s_bfe_u32 s16, s2, 0x20001
	s_mul_i32 s2, s16, 0xc0
	s_lshl_b32 s12, s14, 1
	s_add_i32 s17, s15, s2
	s_load_dwordx8 s[4:11], s[0:1], 0x0
	s_and_b32 s12, s12, -16
	s_lshl_b32 s13, s14, 4
	s_and_b32 s13, s13, 0x70
	s_mov_b32 s3, 0
	v_mov_b32_e32 v32, 0
	v_lshrrev_b32_e32 v78, 6, v0
	v_bfe_u32 v65, v0, 2, 4
	v_lshlrev_b32_e32 v1, 4, v0
	v_and_b32_e32 v30, 48, v1
	v_lshl_add_u32 v1, v78, 7, v65
	v_lshl_add_u32 v1, v1, 9, v30
	s_lshl_b32 s18, s17, 7
	s_add_i32 s18, s18, s12
	s_lshl_b32 s18, s18, 9
	s_lshl_b32 s2, s13, 2
	s_add_i32 s18, s18, s2
	s_waitcnt lgkmcnt(0)
	s_add_u32 s20, s4, s18
	s_addc_u32 s21, s5, 0
	s_add_u32 s22, s20, 0x40000
	s_addc_u32 s23, s21, 0
	s_add_u32 s24, s22, 0x40000
	s_addc_u32 s25, s23, 0
	s_add_u32 s26, s24, 0x40000
	s_addc_u32 s27, s25, 0
	s_add_u32 s28, s26, 0x40000
	s_addc_u32 s29, s27, 0
	s_add_u32 s30, s28, 0x40000
	s_addc_u32 s31, s29, 0
	s_add_u32 s32, s30, 0x40000
	s_addc_u32 s33, s31, 0
	s_add_u32 s34, s32, 0x40000
	s_addc_u32 s35, s33, 0
	v_readfirstlane_b32 s19, v78
	s_nop 3
	s_mul_i32 s19, s19, 0x410
	s_add_i32 m0, s19, 29120
	s_nop 0
	global_load_lds_dwordx4 v1, s[34:35]
	s_add_i32 m0, s19, 24960
	s_nop 0
	global_load_lds_dwordx4 v1, s[32:33]
	s_add_i32 m0, s19, 20800
	s_nop 0
	global_load_lds_dwordx4 v1, s[30:31]
	s_add_i32 m0, s19, 16640
	s_nop 0
	global_load_lds_dwordx4 v1, s[28:29]
	s_add_i32 m0, s19, 12480
	s_nop 0
	global_load_lds_dwordx4 v1, s[26:27]
	s_add_i32 m0, s19, 8320
	s_nop 0
	global_load_lds_dwordx4 v1, s[24:25]
	v_bfe_u32 v103, v0, 5, 1
	v_lshrrev_b32_e32 v33, 2, v0
	s_add_i32 m0, s19, 4160
	s_nop 0
	global_load_lds_dwordx4 v1, s[22:23]
	s_mov_b32 m0, s19
	s_nop 0
	global_load_lds_dwordx4 v1, s[20:21]
	v_lshlrev_b32_e32 v104, 1, v78
	v_and_b32_e32 v27, 3, v0
	v_lshrrev_b32_e32 v28, 1, v0
	v_and_or_b32 v59, v33, 1, v104
	v_and_or_b32 v105, v28, 12, v27
	v_lshlrev_b32_e32 v28, 4, v103
	v_mov_b32_e32 v29, v32
	v_lshl_add_u64 v[56:57], s[6:7], 0, v[28:29]
	v_or_b32_e32 v27, s13, v59
	v_or_b32_e32 v28, s12, v105
	s_lshl_b32 s4, s16, 16
	v_lshl_add_u32 v31, v27, 7, v28
	s_or_b32 s2, s4, 0x4000
	v_add_u32_e32 v27, 0x400, v31
	s_or_b32 s5, s4, 0xc000
	v_add_u32_e32 v28, s2, v27
	v_and_b32_e32 v1, 31, v0
	v_ashrrev_i32_e32 v29, 31, v28
	v_add_u32_e32 v34, s5, v27
	v_or_b32_e32 v26, s15, v1
	v_lshlrev_b64 v[28:29], 5, v[28:29]
	v_ashrrev_i32_e32 v35, 31, v34
	v_lshl_add_u64 v[28:29], v[56:57], 0, v[28:29]
	v_lshlrev_b64 v[34:35], 5, v[34:35]
	v_lshl_or_b32 v58, v26, 1, v103
	v_lshl_add_u64 v[34:35], v[56:57], 0, v[34:35]
	global_load_dwordx4 v[36:39], v[28:29], off
	global_load_dwordx4 v[40:43], v[34:35], off
	v_add_u32_e32 v28, 0x180, v58
	v_ashrrev_i32_e32 v29, 31, v28
	v_add_u32_e32 v34, 0x480, v58
	v_lshl_add_u64 v[28:29], v[28:29], 4, s[8:9]
	v_ashrrev_i32_e32 v35, 31, v34
	v_ashrrev_i32_e32 v27, 31, v26
	v_lshl_add_u64 v[34:35], v[34:35], 4, s[8:9]
	global_load_dwordx4 v[44:47], v[28:29], off
	global_load_dwordx4 v[48:51], v[34:35], off
	v_lshl_add_u64 v[60:61], v[26:27], 2, s[10:11]
	v_add_u32_e32 v26, s5, v31
	v_add_u32_e32 v28, s2, v31
	v_ashrrev_i32_e32 v27, 31, v26
	v_ashrrev_i32_e32 v29, 31, v28
	v_lshlrev_b64 v[26:27], 5, v[26:27]
	v_lshlrev_b64 v[28:29], 5, v[28:29]
	global_load_dword v62, v[60:61], off offset:768
	global_load_dword v64, v[60:61], off offset:2304
	v_lshl_add_u64 v[26:27], v[56:57], 0, v[26:27]
	v_lshl_add_u64 v[28:29], v[56:57], 0, v[28:29]
	global_load_dwordx4 v[52:55], v[26:27], off
	s_nop 0
	global_load_dwordx4 v[26:29], v[28:29], off
	s_load_dwordx2 s[0:1], s[0:1], 0x28
	v_and_b32_e32 v0, 63, v0
	v_bfrev_b32_e32 v31, 60
	v_cmp_gt_u32_e32 vcc, 32, v0
	v_mul_u32_u24_e32 v102, 0x410, v1
	v_lshlrev_b32_e32 v0, 2, v1
	v_mov_b32_e32 v1, v32
	v_cndmask_b32_e64 v34, v31, 0, vcc
	s_waitcnt lgkmcnt(0)
	v_lshl_add_u64 v[72:73], s[0:1], 0, v[0:1]
	v_mul_u32_u24_e32 v0, 0x410, v78
	v_lshlrev_b32_e32 v1, 6, v65
	v_add3_u32 v1, v0, v1, v30
	s_mul_i32 s16, s16, 24
	s_lshr_b32 s0, s15, 5
	s_waitcnt vmcnt(8)
	s_add_i32 s0, s0, s16
	s_waitcnt lgkmcnt(0)
	s_barrier
	s_lshl_b32 s2, s0, 10
	v_mov_b32_e32 v33, v32
	v_mov_b32_e32 v35, v32
	v_lshl_or_b32 v106, v103, 2, v102
	s_add_i32 s5, s2, 0x4800
	v_or_b32_e32 v107, s13, v103
	s_ashr_i32 s6, s14, 3
	s_add_i32 s7, s2, 0x1800
	s_mov_b64 s[0:1], -1
	s_mov_b32 s10, 0x7f61b1e6
	s_mov_b32 s11, 0x42800000
	s_waitcnt vmcnt(3)
	v_mov_b32_e32 v63, v62
	s_waitcnt vmcnt(2)
	v_mov_b32_e32 v65, v64
	s_waitcnt vmcnt(0)
	s_branch .LBB2_3

.Lstag_done_p3:
	s_mov_b32 s66, s2
	s_load_dwordx2 s[64:65], s[0:1], 0x0
	v_lshrrev_b32_e32 v162, 6, v0
	v_bfe_u32 v163, v0, 2, 4
	v_lshl_add_u32 v162, v162, 7, v163
	v_lshlrev_b32_e32 v163, 4, v0
	v_and_b32_e32 v163, 48, v163
	v_lshl_add_u32 v162, v162, 9, v163
	s_load_dwordx8 s[4:11], s[0:1], 0x0
	s_load_dwordx2 s[16:17], s[0:1], 0x20
	s_load_dwordx4 s[12:15], s[0:1], 0x30
	s_ashr_i32 s0, s2, 3
	s_mul_hi_i32 s18, s0, 0x55555556
	s_lshr_b32 s19, s18, 31
	s_add_i32 s21, s18, s19
	s_mul_i32 s18, s21, 0x3fffffd
	s_bfe_u32 s1, s2, 0x20001
	s_add_i32 s18, s18, s0
	s_lshl_b32 s2, s2, 5
	s_lshl_b32 s0, s18, 6
	s_and_b32 s2, s2, 32
	s_or_b32 s0, s0, s2
	s_lshl_b32 s2, s21, 1
	s_and_b32 s19, s2, -16
	s_lshl_b32 s2, s21, 4
	s_and_b32 s20, s2, 0x70
	s_mul_i32 s2, s1, 0xc0
	s_add_i32 s18, s0, s2
	s_mov_b32 s3, 0
	v_mov_b32_e32 v50, 0
	v_lshrrev_b32_e32 v142, 6, v0
	v_bfe_u32 v45, v0, 2, 4
	v_lshlrev_b32_e32 v1, 4, v0
	v_and_b32_e32 v34, 48, v1
	v_lshl_add_u32 v1, v142, 7, v45
	v_lshl_add_u32 v1, v1, 9, v34
	s_lshl_b32 s22, s18, 7
	s_add_i32 s22, s22, s19
	s_lshl_b32 s22, s22, 9
	s_lshl_b32 s2, s20, 2
	s_add_i32 s22, s22, s2
	s_waitcnt lgkmcnt(0)
	s_add_u32 s24, s4, s22
	s_addc_u32 s25, s5, 0
	s_add_u32 s26, s24, 0x40000
	s_addc_u32 s27, s25, 0
	s_add_u32 s28, s26, 0x40000
	s_addc_u32 s29, s27, 0
	s_add_u32 s30, s28, 0x40000
	s_addc_u32 s31, s29, 0
	s_add_u32 s32, s30, 0x40000
	s_addc_u32 s33, s31, 0
	s_add_u32 s34, s32, 0x40000
	s_addc_u32 s35, s33, 0
	s_add_u32 s36, s34, 0x40000
	s_addc_u32 s37, s35, 0
	s_add_u32 s38, s36, 0x40000
	s_addc_u32 s39, s37, 0
	v_readfirstlane_b32 s23, v142
	s_nop 3
	s_mul_i32 s23, s23, 0x410
	s_add_i32 m0, s23, 29120
	s_nop 0
	global_load_lds_dwordx4 v1, s[38:39]
	s_add_i32 m0, s23, 24960
	s_nop 0
	global_load_lds_dwordx4 v1, s[36:37]
	s_add_i32 m0, s23, 20800
	s_nop 0
	global_load_lds_dwordx4 v1, s[34:35]
	s_add_i32 m0, s23, 16640
	s_nop 0
	global_load_lds_dwordx4 v1, s[32:33]
	s_add_i32 m0, s23, 12480
	s_nop 0
	global_load_lds_dwordx4 v1, s[30:31]
	s_add_i32 m0, s23, 8320
	s_nop 0
	global_load_lds_dwordx4 v1, s[28:29]
	v_and_b32_e32 v35, 31, v0
	s_add_i32 m0, s23, 4160
	s_nop 0
	global_load_lds_dwordx4 v1, s[26:27]
	s_mov_b32 m0, s23
	s_nop 0
	global_load_lds_dwordx4 v1, s[24:25]
	v_or_b32_e32 v36, s0, v35
	v_ashrrev_i32_e32 v37, 31, v36
	v_lshlrev_b64 v[38:39], 2, v[36:37]
	v_lshlrev_b32_e32 v89, 1, v142
	v_and_b32_e32 v1, 3, v0
	v_lshrrev_b32_e32 v37, 1, v0
	v_lshl_add_u64 v[40:41], s[16:17], 0, v[38:39]
	v_and_or_b32 v144, v37, 12, v1
	v_or_b32_e32 v1, s20, v89
	global_load_dword v94, v[40:41], off
	v_bfe_u32 v143, v0, 2, 1
	v_lshlrev_b32_e32 v40, 1, v35
	v_mov_b32_e32 v41, v50
	v_or_b32_e32 v37, 8, v1
	v_bfe_u32 v95, v0, 5, 1
	s_lshl_b32 s4, s1, 16
	v_lshl_add_u64 v[86:87], s[12:13], 0, v[40:41]
	v_or_b32_e32 v51, s19, v144
	v_or_b32_e32 v40, v37, v143
	v_lshlrev_b32_e32 v82, 4, v95
	v_mov_b32_e32 v83, v50
	s_ashr_i32 s5, s0, 5
	s_or_b32 s0, s4, 0x4000
	v_lshl_add_u32 v42, v40, 7, v51
	v_lshl_add_u64 v[84:85], s[6:7], 0, v[82:83]
	s_or_b32 s2, s4, 0xc000
	s_mul_i32 s7, s1, 24
	v_add_u32_e32 v40, s0, v42
	s_or_b32 s1, s7, 6
	v_ashrrev_i32_e32 v41, 31, v40
	v_add_u32_e32 v42, s2, v42
	s_add_i32 s6, s5, 12
	s_ashr_i32 s12, s21, 3
	s_add_i32 s13, s1, s5
	v_lshlrev_b64 v[40:41], 5, v[40:41]
	v_ashrrev_i32_e32 v43, 31, v42
	v_or_b32_e32 v37, v37, v95
	s_lshl_b32 s13, s13, 10
	s_add_i32 s1, s1, s6
	v_lshl_add_u64 v[40:41], v[84:85], 0, v[40:41]
	v_lshlrev_b64 v[42:43], 5, v[42:43]
	v_lshl_add_u32 v37, v37, 3, s12
	s_lshl_b32 s1, s1, 10
	v_lshl_add_u64 v[42:43], v[84:85], 0, v[42:43]
	global_load_dwordx4 v[58:61], v[40:41], off
	global_load_dwordx4 v[62:65], v[42:43], off
	v_add_u32_e32 v40, s13, v37
	v_ashrrev_i32_e32 v41, 31, v40
	v_add_u32_e32 v42, s1, v37
	v_lshlrev_b64 v[40:41], 6, v[40:41]
	v_ashrrev_i32_e32 v43, 31, v42
	v_lshl_or_b32 v88, v36, 1, v95
	v_lshl_add_u64 v[40:41], v[86:87], 0, v[40:41]
	v_lshlrev_b64 v[42:43], 6, v[42:43]
	v_add_u32_e32 v36, 0x180, v88
	v_lshl_add_u64 v[42:43], v[86:87], 0, v[42:43]
	global_load_ushort v145, v[40:41], off
	global_load_ushort v146, v[42:43], off
	v_ashrrev_i32_e32 v37, 31, v36
	v_add_u32_e32 v40, 0x480, v88
	v_lshl_add_u64 v[36:37], v[36:37], 4, s[8:9]
	v_ashrrev_i32_e32 v41, 31, v40
	v_lshl_add_u64 v[40:41], v[40:41], 4, s[8:9]
	global_load_dwordx4 v[66:69], v[36:37], off
	global_load_dwordx4 v[70:73], v[40:41], off
	v_or_b32_e32 v36, v1, v95
	v_lshl_add_u64 v[90:91], s[10:11], 0, v[38:39]
	v_lshl_add_u32 v38, v36, 3, s12
	v_add_u32_e32 v36, s1, v38
	v_ashrrev_i32_e32 v37, 31, v36
	v_add_u32_e32 v38, s13, v38
	v_lshlrev_b64 v[36:37], 6, v[36:37]
	v_ashrrev_i32_e32 v39, 31, v38
	v_or_b32_e32 v1, v1, v143
	v_lshl_add_u64 v[36:37], v[86:87], 0, v[36:37]
	v_lshlrev_b64 v[38:39], 6, v[38:39]
	v_lshl_add_u32 v1, v1, 7, v51
	global_load_dword v92, v[90:91], off offset:2304
	global_load_dword v96, v[90:91], off offset:768
	v_lshl_add_u64 v[38:39], v[86:87], 0, v[38:39]
	global_load_ushort v150, v[36:37], off
	global_load_ushort v151, v[38:39], off
	v_add_u32_e32 v36, s2, v1
	v_ashrrev_i32_e32 v37, 31, v36
	v_add_u32_e32 v38, s0, v1
	v_lshlrev_b64 v[36:37], 5, v[36:37]
	v_ashrrev_i32_e32 v39, 31, v38
	v_lshl_add_u64 v[36:37], v[84:85], 0, v[36:37]
	v_lshlrev_b64 v[38:39], 5, v[38:39]
	v_lshl_add_u64 v[38:39], v[84:85], 0, v[38:39]
	global_load_dwordx4 v[74:77], v[36:37], off
	global_load_dwordx4 v[78:81], v[38:39], off
	v_and_b32_e32 v1, 63, v0
	v_cmp_gt_u32_e32 vcc, 32, v1
	v_bfrev_b32_e32 v1, 60
	v_mul_u32_u24_e32 v83, 0x210, v35
	v_mov_b32_e32 v36, 0x3c00
	v_cndmask_b32_e64 v56, v1, 0, vcc
	v_mul_u32_u24_e32 v1, 0x410, v35
	v_lshl_or_b32 v35, v95, 1, v83
	v_cndmask_b32_e64 v53, v36, 0, vcc
	v_add_u32_e32 v148, 0x8200, v35
	v_mul_u32_u24_e32 v35, 0x410, v142
	v_lshlrev_b32_e32 v36, 6, v45
	v_add3_u32 v34, v35, v36, v34
	s_waitcnt vmcnt(13)
	s_waitcnt lgkmcnt(0)
	s_barrier
	v_mov_b32_e32 v51, v50
	v_mov_b32_e32 v52, v50
	v_mov_b32_e32 v54, v50
	v_mov_b32_e32 v55, v50
	v_mov_b32_e32 v57, v50
	v_lshl_or_b32 v147, v95, 2, v1
	s_mov_b64 s[0:1], -1
	s_mov_b32 s10, 0x7f61b1e6
	s_mov_b32 s11, 0x42800000
	s_waitcnt vmcnt(5)
	v_mov_b32_e32 v93, v92
	s_waitcnt vmcnt(4)
	v_mov_b32_e32 v97, v96
	s_branch .LBB3_3
